# mLSTM scan waves run at raised issue priority (s_setprio 3) over the co-resident RWKV waves; priority reset before the weight conversion
# speedup vs baseline: 1.0079x; 1.0065x over previous
; #define LAS __attribute__((address_space(3)))
; __device__ __forceinline__ void mlstm_scan_unit(Frame& F, int unit, LAS unsigned* bcnt, unsigned& btarget) {
;     const int b = unit >> 5, mh = (unit >> 3) & 3, sl = unit & 7;
;     const bf16* P = (const bf16*)(F.ws + WS_P); const bf16* QKC = (const bf16*)(F.ws + WS_QKC); const float* GLF = (const float*)(F.ws + WS_GLF); float* HRAW = (float*)(F.ws + WS_HRAW);
;     constexpr int VS = 56;
;     LAS bf16* Lq = (LAS bf16*)F.lds;
;     LAS bf16* Lk = Lq + 64 * 136;
;     LAS bf16* Lv = Lk + 64 * 136;
;     LAS bf16* Lvs = Lv + 64 * VS;
;     LAS bf16* LcT = Lvs + 64 * VS;
;     LAS bf16* Ls = LcT + 2 * 48 * 136;
;     LAS float* sb = (LAS float*)(Ls + 64 * 72); LAS float* su = sb + 64; LAS float* smx = su + 64; LAS float* swk = smx + 64;
;     const int tid = F.tid, lane = F.lane, w = F.wave, fr = lane & 15, fq = lane >> 4;
;     for (int i = tid; i < 2 * 48 * 136; i += 256) LcT[i] = 0;
;     for (int i = tid; i < 64 * 16; i += 256) { const int j = i >> 4, c = 32 + (i & 15); Lv[j * VS + c] = (c == 32) ? (bf16)0x3F80 : (bf16)0; Lvs[j * VS + c] = 0; }
;     const int pr0 = tid >> 4, pc = 8 * (tid & 15);
;     v4u rq[4], rk[4], rv; f32x4 g3;
;     ...
;     f32x4 st[2][3];
; #pragma unroll
;     for (int a = 0; a < 2; ++a)
; #pragma unroll
;         for (int n = 0; n < 3; ++n) st[a][n] = (f32x4){0.f, 0.f, 0.f, 0.f};
;     float mstate = 0.f;
;     ML_LOAD(0);
;     rw_bar(bcnt, btarget, lane);
.LBB0_905:
	v_readlane_b32 s0, v237, 50
	v_readlane_b32 s1, v237, 51
	s_cmp_lt_i32 s0, 5
	s_cselect_b64 s[0:1], -1, 0
	s_and_b64 s[0:1], s[0:1], s[2:3]
	v_writelane_b32 v237, s0, 57
	s_andn2_b64 vcc, exec, s[0:1]
	s_nop 0
	v_writelane_b32 v237, s1, 58
	s_cbranch_vccnz .LBB0_1097
	s_mov_b32 s64, s72
	s_cmpk_gt_u32 s93, 0xff
	s_mov_b64 s[0:1], -1
	v_writelane_b32 v237, s64, 59
	s_nop 1
	v_writelane_b32 v237, s65, 60
	s_cbranch_scc0 .LBB0_964
	s_cmpk_gt_i32 s74, 0xff
	s_mov_b32 s1, 0
	v_cmp_eq_u32_e64 s[4:5], 0, v162
	s_mov_b32 s6, 4
	s_cbranch_scc1 .LBB0_956
	s_add_i32 s0, s92, -4
	s_add_u32 s2, s90, 0x38200000
	s_waitcnt vmcnt(4)
	v_add_u32_e32 v3, 0xffffff00, v0
	s_addc_u32 s3, s91, 0
	s_add_u32 s40, s90, 0x6a200000
	v_lshlrev_b32_e32 v4, 4, v3
	s_addc_u32 s41, s91, 0
	v_and_b32_e32 v82, 0xf0, v4
	v_mov_b32_e32 v83, 0
	s_add_u32 s33, s90, 0x5e200000
	v_lshl_add_u64 v[4:5], s[90:91], 0, v[82:83]
	s_mov_b64 s[6:7], 0x66200000
	s_addc_u32 s64, s91, 0
	s_waitcnt vmcnt(3)
	v_lshlrev_b32_e32 v6, 3, v3
	v_ashrrev_i32_e32 v80, 4, v3
	v_lshl_add_u64 v[84:85], v[4:5], 0, s[6:7]
	v_ashrrev_i32_e32 v86, 2, v3
	s_add_i32 s8, 0, 0x1fa00
	s_add_i32 s9, 0, 0x1fb00
	s_add_i32 s10, 0, 0x1fc00
	s_add_i32 s6, 0, 0x1fd00
	v_and_b32_e32 v3, -4, v3
	v_and_b32_e32 v4, 24, v6
	v_lshlrev_b32_e32 v5, 2, v162
	s_cmp_eq_u32 s0, 0
	v_add_u32_e32 v105, s6, v3
	v_mul_i32_i24_e32 v3, 56, v86
	v_and_b32_e32 v2, 15, v0
	v_add_u32_e32 v79, s8, v5
	v_add_u32_e32 v101, s9, v5
	v_add_u32_e32 v102, s10, v5
	v_add_u32_e32 v103, s6, v5
	s_cselect_b64 s[42:43], -1, 0
	s_add_i32 s11, 0, 0x13800
	v_lshlrev_b32_e32 v5, 1, v4
	s_add_i32 s65, 0, 0x15400
	v_lshlrev_b32_e32 v3, 1, v3
	s_lshl_b32 s14, s0, 4
	v_lshrrev_b32_e32 v7, 4, v162
	v_add3_u32 v106, s11, v5, v3
	v_add3_u32 v107, s65, v5, v3
	v_or_b32_e32 v3, s14, v2
	s_movk_i32 s6, 0x90
	v_mul_lo_u32 v5, v3, s6
	s_add_i32 s6, 0, 0x1d600
	v_lshlrev_b32_e32 v109, 3, v7
	v_add3_u32 v110, s6, v5, v109
	v_and_b32_e32 v5, 48, v162
	v_add_u32_e32 v6, 0, v5
	s_movk_i32 s15, 0x110
	v_mad_u64_u32 v[88:89], s[6:7], v3, s15, v[6:7]
	v_lshlrev_b32_e32 v7, 2, v7
	v_bfe_u32 v8, v0, 2, 2
	v_and_b32_e32 v9, 12, v163
	s_lshl_b32 s0, s0, 6
	v_lshl_add_u32 v108, v3, 2, s10
	v_or_b32_e32 v8, v109, v8
	v_lshlrev_b32_e32 v9, 1, v9
	s_add_i32 s10, s10, s0
	v_mad_u32_u24 v115, v2, s15, v6
	v_or_b32_e32 v6, 3, v7
	s_waitcnt vmcnt(1)
	v_or_b32_e32 v14, 2, v7
	v_mov_b32_e32 v15, 0x2200
	v_add_u32_e32 v10, s11, v9
	v_add_u32_e32 v111, s10, v5
	s_ashr_i32 s16, s14, 31
	v_cmp_gt_i32_e64 s[10:11], v6, v3
	v_cmp_gt_i32_e64 s[12:13], v14, v3
	v_mul_u32_u24_e32 v6, 0x70, v8
	v_mul_u32_u24_e32 v14, 0x110, v8
	v_mad_u32_u24 v8, v8, s15, v15
	v_or_b32_e32 v15, 16, v7
	v_or_b32_e32 v16, 17, v7
	v_or_b32_e32 v17, 18, v7
	s_add_i32 s50, 0, 0x17000
	s_add_i32 s8, s8, s0
	s_add_i32 s6, s0, 0
	v_mul_i32_i24_e32 v13, 0x88, v80
	v_mov_b32_e32 v91, s16
	v_or_b32_e32 v18, 19, v7
	v_cmp_gt_i32_e64 s[16:17], v17, v3
	v_cmp_gt_i32_e64 s[18:19], v16, v3
	v_cmp_gt_i32_e64 s[20:21], v15, v3
	v_or_b32_e32 v15, 32, v7
	v_or_b32_e32 v16, 33, v7
	v_or_b32_e32 v17, 34, v7
	v_add_u32_e32 v89, s9, v5
	v_add_u32_e32 v112, s8, v5
	v_add_u32_e32 v12, s6, v9
	s_add_i32 s0, s50, s0
	v_lshlrev_b32_e32 v13, 1, v13
	v_cmp_gt_i32_e64 s[6:7], v7, v3
	v_cmp_lt_i32_e64 s[8:9], v7, v3
	v_or_b32_e32 v90, s14, v7
	v_cmp_gt_i32_e64 s[14:15], v18, v3
	v_or_b32_e32 v18, 35, v7
	v_cmp_gt_i32_e64 s[24:25], v17, v3
	v_cmp_gt_i32_e64 s[26:27], v16, v3
	v_cmp_gt_i32_e64 s[28:29], v15, v3
	v_or_b32_e32 v15, 48, v7
	v_or_b32_e32 v16, 49, v7
	v_or_b32_e32 v17, 50, v7
	v_or_b32_e32 v7, 51, v7
	v_or_b32_e32 v78, 32, v2
	v_cmp_eq_u32_e32 vcc, 0, v2
	v_add3_u32 v113, 0, v82, v13
	v_mul_u32_u24_e32 v13, 0x110, v2
	s_cmpk_gt_u32 s93, 0x13f
	v_cmp_gt_i32_e64 s[22:23], v18, v3
	v_cmp_gt_i32_e64 s[30:31], v7, v3
	v_cmp_gt_i32_e64 s[34:35], v17, v3
	v_cmp_gt_i32_e64 s[36:37], v16, v3
	v_cmp_gt_i32_e64 s[38:39], v15, v3
	v_lshl_add_u32 v3, v0, 1, 0
	v_lshlrev_b32_e32 v92, 2, v2
	v_mbcnt_lo_u32_b32 v2, -1, 0
	v_and_b32_e32 v11, 48, v0
	s_cselect_b64 s[44:45], -1, 0
	s_cmpk_gt_u32 s93, 0x17f
	v_add_u32_e32 v120, 0x16e00, v3
	v_mbcnt_hi_u32_b32 v2, -1, v2
	v_bfrev_b32_e32 v3, 0.5
	v_mov_b32_e32 v1, 0x3f80
	v_add_u32_e32 v9, s65, v9
	s_cselect_b64 s[46:47], -1, 0
	s_cmpk_gt_u32 s93, 0x1bf
	v_lshl_or_b32 v125, v2, 2, v3
	v_and_or_b32 v2, v2, 64, v11
	v_cndmask_b32_e32 v1, 0, v1, vcc
	v_ashrrev_i32_e32 v81, 31, v80
	v_ashrrev_i32_e32 v87, 31, v86
	v_mul_u32_u24_e32 v104, 0x70, v162
	v_add_u32_e32 v114, 0xf400, v113
	v_add_u32_e32 v116, 0xf400, v115
	s_cselect_b64 s[48:49], -1, 0
	v_add3_u32 v117, s50, v5, v13
	v_add3_u32 v118, s0, v109, v13
	v_or_b32_e32 v119, 0xfffffe00, v0
	s_movk_i32 s66, 0x5400
	v_lshlrev_b32_e32 v82, 1, v4
	s_add_i32 s67, 0, 0x20048
	v_add_u32_e32 v121, v10, v6
	v_add_u32_e32 v122, v12, v14
	v_add_u32_e32 v123, v9, v6
	v_add_u32_e32 v124, v12, v8
	v_lshlrev_b32_e32 v126, 2, v2
	s_mov_b32 s68, s74
	s_mov_b32 s0, 0
	s_setprio 3
	s_branch .LBB0_910

; #define TP_B(k) do { if ((k) == TPROBE % 100) tpB = __builtin_amdgcn_s_memrealtime(); } while (0)
; #define TP_B(k) do {} while (0)
; __global__ void __launch_bounds__(NTHR, 2) mk_fwd(Args args) {
;     ...
;                  for (int rep = 0; rep < REP(41); ++rep) for (int u = F.bid; u < 256; u += F.G) mlstm_scan_unit(F2, u, ctl2 + 2, bt);
;                  rw_bar(ctl2 + 2, bt, F2.lane); TP_B(15); TP_B(16); }
;           if (F.wave >= CV_W0) convert_loop(F, F.ctl + CW_CVNEXT, nullptr, 0u, F.lds + 45056 + (F.wave - 4) * 9216, 0u, (unsigned)CV_SPLIT);
.LBB0_955:
	s_setprio 0
	s_add_i32 s6, s69, 0x188
